# speedup vs baseline: 1.0381x; 1.0185x over previous
.LBB0_16:
	s_load_dwordx2 s[4:5], s[0:1], 0x0
	s_mul_i32 s3, s2, 0x7a2
	v_add_u32_e32 v2, s3, v0
	v_mov_b32_e32 v1, -1
	v_mov_b32_e32 v6, -1
	s_waitcnt lgkmcnt(0)
	s_add_u32 s4, s4, 0x1e8480
	s_addc_u32 s5, s5, 0
	s_min_i32 s3, s3, 0x7997e
	s_addk_i32 s3, 0x7a2
	v_cmp_gt_i32_e32 vcc, s3, v2
	s_and_saveexec_b64 s[6:7], vcc
	s_cbranch_execz .LBB0_18
	v_ashrrev_i32_e32 v3, 31, v2
	v_lshl_add_u64 v[4:5], v[2:3], 2, s[4:5]
	global_load_dword v6, v[4:5], off nt
.LBB0_18:
	s_or_b64 exec, exec, s[6:7]
	v_add_u32_e32 v4, 0x200, v2
	v_cmp_gt_i32_e32 vcc, s3, v4
	s_and_saveexec_b64 s[6:7], vcc
	s_cbranch_execz .LBB0_20
	v_ashrrev_i32_e32 v5, 31, v4
	v_lshl_add_u64 v[4:5], v[4:5], 2, s[4:5]
	global_load_dword v1, v[4:5], off nt
.LBB0_20:
	s_or_b64 exec, exec, s[6:7]
	v_add_u32_e32 v4, 0x400, v2
	v_cmp_gt_i32_e32 vcc, s3, v4
	v_mov_b32_e32 v3, -1
	v_mov_b32_e32 v5, -1
	s_and_saveexec_b64 s[6:7], vcc
	s_cbranch_execz .LBB0_22
	v_ashrrev_i32_e32 v5, 31, v4
	v_lshl_add_u64 v[4:5], v[4:5], 2, s[4:5]
	global_load_dword v5, v[4:5], off nt
.LBB0_22:
	s_or_b64 exec, exec, s[6:7]
	v_add_u32_e32 v2, 0x600, v2
	v_cmp_gt_i32_e32 vcc, s3, v2
	s_and_saveexec_b64 s[6:7], vcc
	s_cbranch_execz .LBB0_24
	v_ashrrev_i32_e32 v3, 31, v2
	v_lshl_add_u64 v[2:3], v[2:3], 2, s[4:5]
	global_load_dword v3, v[2:3], off nt

_Z14k_scatter_nodePKiS0_PjPiPKfS4_PfS5_PDF16_:
	s_mov_b32 s31, s2
	s_mov_b64 s[34:35], s[0:1]
	s_cmpk_gt_i32 s2, 0xff
	s_mov_b64 s[4:5], -1
	s_cbranch_scc0 .LBB1_4
	s_load_dwordx8 s[12:19], s[34:35], 0x20
	s_load_dwordx2 s[20:21], s[34:35], 0x40
	v_lshrrev_b32_e32 v1, 6, v0
	v_and_b32_e32 v3, 15, v0
	v_bfe_u32 v4, v0, 4, 2
	s_lshl_b32 s3, s31, 8
	s_add_i32 s3, s3, 0xffff0000
	v_lshl_add_u32 v5, v1, 5, s3
	v_add_u32_e32 v6, v5, v3
	v_readfirstlane_b32 s22, v5
	v_add_u32_e32 v7, 16, v6
	s_mov_b32 s23, 0xc350
	s_cmp_ge_i32 s22, s23
	s_cbranch_scc1 .Lk2n_end
	v_min_i32_e32 v8, 0xc34f, v6
	v_min_i32_e32 v9, 0xc34f, v7
	v_lshlrev_b32_e32 v10, 4, v4
	v_lshl_add_u32 v8, v8, 8, v10
	v_lshl_add_u32 v9, v9, 8, v10
	v_lshlrev_b32_e32 v11, 2, v3
	v_lshl_add_u32 v11, v4, 8, v11
	s_waitcnt lgkmcnt(0)
	global_load_dwordx4 v[32:35], v8, s[12:13] nt
	global_load_dwordx4 v[36:39], v8, s[12:13] offset:64 nt
	global_load_dwordx4 v[40:43], v8, s[12:13] offset:128 nt
	global_load_dwordx4 v[44:47], v8, s[12:13] offset:192 nt
	global_load_dwordx4 v[48:51], v9, s[12:13] nt
	global_load_dwordx4 v[52:55], v9, s[12:13] offset:64 nt
	global_load_dwordx4 v[56:59], v9, s[12:13] offset:128 nt
	global_load_dwordx4 v[60:63], v9, s[12:13] offset:192 nt
	global_load_dword v16, v11, s[14:15]
	global_load_dword v17, v11, s[14:15] offset:64
	global_load_dword v18, v11, s[14:15] offset:128
	global_load_dword v19, v11, s[14:15] offset:192
	global_load_dword v20, v11, s[14:15] offset:1024
	global_load_dword v21, v11, s[14:15] offset:1088
	global_load_dword v22, v11, s[14:15] offset:1152
	global_load_dword v23, v11, s[14:15] offset:1216
	global_load_dword v24, v11, s[14:15] offset:2048
	global_load_dword v25, v11, s[14:15] offset:2112
	global_load_dword v26, v11, s[14:15] offset:2176
	global_load_dword v27, v11, s[14:15] offset:2240
	global_load_dword v28, v11, s[14:15] offset:3072
	global_load_dword v29, v11, s[14:15] offset:3136
	global_load_dword v30, v11, s[14:15] offset:3200
	global_load_dword v31, v11, s[14:15] offset:3264
	v_cmp_gt_i32_e64 s[24:25], s23, v6
	v_cmp_gt_i32_e64 s[26:27], s23, v7
	v_cmp_gt_u32_e32 vcc, 2, v4
	v_mov_b32_e32 v12, s18
	v_mov_b32_e32 v13, s19
	v_mov_b32_e32 v14, s16
	v_mov_b32_e32 v15, s17
	v_cndmask_b32_e32 v12, v12, v14, vcc
	v_cndmask_b32_e32 v13, v13, v15, vcc
	v_and_b32_e32 v14, 1, v4
	v_lshlrev_b32_e32 v14, 4, v14
	v_mov_b32_e32 v15, 0
	v_lshl_add_u32 v88, v6, 5, v14
	v_mov_b32_e32 v89, 0
	v_lshl_add_u32 v14, v7, 5, v14
	v_lshl_add_u64 v[88:89], v[88:89], 0, v[12:13]
	v_lshl_add_u64 v[90:91], v[14:15], 0, v[12:13]
	v_lshlrev_b32_e32 v10, 3, v4
	v_lshl_add_u32 v92, v6, 7, v10
	v_lshl_add_u32 v93, v7, 7, v10
	s_waitcnt vmcnt(0)
	v_mfma_f32_16x16x4_f32 v[64:67], v16, v32, 0
	v_mfma_f32_16x16x4_f32 v[68:71], v16, v48, 0
	v_mfma_f32_16x16x4_f32 v[64:67], v17, v33, v[64:67]
	v_mfma_f32_16x16x4_f32 v[68:71], v17, v49, v[68:71]
	v_mfma_f32_16x16x4_f32 v[64:67], v18, v34, v[64:67]
	v_mfma_f32_16x16x4_f32 v[68:71], v18, v50, v[68:71]
	v_mfma_f32_16x16x4_f32 v[64:67], v19, v35, v[64:67]
	v_mfma_f32_16x16x4_f32 v[68:71], v19, v51, v[68:71]
	v_mfma_f32_16x16x4_f32 v[64:67], v20, v36, v[64:67]
	v_mfma_f32_16x16x4_f32 v[68:71], v20, v52, v[68:71]
	v_mfma_f32_16x16x4_f32 v[64:67], v21, v37, v[64:67]
	v_mfma_f32_16x16x4_f32 v[68:71], v21, v53, v[68:71]
	v_mfma_f32_16x16x4_f32 v[64:67], v22, v38, v[64:67]
	v_mfma_f32_16x16x4_f32 v[68:71], v22, v54, v[68:71]
	v_mfma_f32_16x16x4_f32 v[64:67], v23, v39, v[64:67]
	v_mfma_f32_16x16x4_f32 v[68:71], v23, v55, v[68:71]
	v_mfma_f32_16x16x4_f32 v[64:67], v24, v40, v[64:67]
	v_mfma_f32_16x16x4_f32 v[68:71], v24, v56, v[68:71]
	v_mfma_f32_16x16x4_f32 v[64:67], v25, v41, v[64:67]
	v_mfma_f32_16x16x4_f32 v[68:71], v25, v57, v[68:71]
	v_mfma_f32_16x16x4_f32 v[64:67], v26, v42, v[64:67]
	v_mfma_f32_16x16x4_f32 v[68:71], v26, v58, v[68:71]
	v_mfma_f32_16x16x4_f32 v[64:67], v27, v43, v[64:67]
	v_mfma_f32_16x16x4_f32 v[68:71], v27, v59, v[68:71]
	v_mfma_f32_16x16x4_f32 v[64:67], v28, v44, v[64:67]
	v_mfma_f32_16x16x4_f32 v[68:71], v28, v60, v[68:71]
	v_mfma_f32_16x16x4_f32 v[64:67], v29, v45, v[64:67]
	v_mfma_f32_16x16x4_f32 v[68:71], v29, v61, v[68:71]
	v_mfma_f32_16x16x4_f32 v[64:67], v30, v46, v[64:67]
	v_mfma_f32_16x16x4_f32 v[68:71], v30, v62, v[68:71]
	v_mfma_f32_16x16x4_f32 v[64:67], v31, v47, v[64:67]
	v_mfma_f32_16x16x4_f32 v[68:71], v31, v63, v[68:71]
	v_cvt_pk_f16_f32 v72, v32, v33
	v_cvt_pk_f16_f32 v73, v34, v35
	v_cvt_pk_f16_f32 v74, v36, v37
	v_cvt_pk_f16_f32 v75, v38, v39
	v_cvt_pk_f16_f32 v76, v40, v41
	v_cvt_pk_f16_f32 v77, v42, v43
	v_cvt_pk_f16_f32 v78, v44, v45
	v_cvt_pk_f16_f32 v79, v46, v47
	v_cvt_pk_f16_f32 v80, v48, v49
	v_cvt_pk_f16_f32 v81, v50, v51
	v_cvt_pk_f16_f32 v82, v52, v53
	v_cvt_pk_f16_f32 v83, v54, v55
	v_cvt_pk_f16_f32 v84, v56, v57
	v_cvt_pk_f16_f32 v85, v58, v59
	v_cvt_pk_f16_f32 v86, v60, v61
	v_cvt_pk_f16_f32 v87, v62, v63
	s_mov_b64 exec, s[24:25]
	global_store_dwordx2 v92, v[72:73], s[20:21]
	global_store_dwordx2 v92, v[74:75], s[20:21] offset:32
	global_store_dwordx2 v92, v[76:77], s[20:21] offset:64
	global_store_dwordx2 v92, v[78:79], s[20:21] offset:96
	global_store_dwordx4 v[88:89], v[64:67], off
	s_mov_b64 exec, s[26:27]
	global_store_dwordx2 v93, v[80:81], s[20:21]
	global_store_dwordx2 v93, v[82:83], s[20:21] offset:32
	global_store_dwordx2 v93, v[84:85], s[20:21] offset:64
	global_store_dwordx2 v93, v[86:87], s[20:21] offset:96
	global_store_dwordx4 v[90:91], v[68:71], off

.LBB1_4:
	s_andn2_b64 vcc, exec, s[4:5]
	s_cbranch_vccnz .LBB1_81
	s_load_dwordx2 s[6:7], s[34:35], 0x0
	s_mul_i32 s3, s31, 0x7a2
	v_add_u32_e32 v2, s3, v0
	v_mov_b32_e32 v1, 0
	v_mov_b32_e32 v102, -1
	s_waitcnt lgkmcnt(0)
	s_add_u32 s8, s6, 0x1e8480
	s_addc_u32 s9, s7, 0
	s_min_i32 s3, s3, 0x7997e
	s_addk_i32 s3, 0x7a2
	v_cmp_gt_i32_e32 vcc, s3, v2
	v_ashrrev_i32_e32 v3, 31, v2
	v_mov_b32_e32 v105, -1
	v_mov_b32_e32 v106, 0
	s_and_saveexec_b64 s[4:5], vcc
	s_cbranch_execz .LBB1_7
	v_lshlrev_b64 v[4:5], 2, v[2:3]
	v_lshl_add_u64 v[6:7], s[8:9], 0, v[4:5]
	v_lshl_add_u64 v[4:5], s[6:7], 0, v[4:5]
	global_load_dword v105, v[6:7], off nt
	global_load_dword v106, v[4:5], off nt
.LBB1_7:
	s_or_b64 exec, exec, s[4:5]
	v_add_u32_e32 v4, 0x200, v2
	v_cmp_gt_i32_e32 vcc, s3, v4
	s_and_saveexec_b64 s[4:5], vcc
	s_cbranch_execz .LBB1_9
	v_ashrrev_i32_e32 v5, 31, v4
	v_lshl_add_u64 v[4:5], v[4:5], 2, s[8:9]
	v_lshl_add_u64 v[6:7], v[2:3], 2, s[6:7]
	global_load_dword v102, v[4:5], off nt
	global_load_dword v1, v[6:7], off offset:2048 nt
.LBB1_9:
	s_or_b64 exec, exec, s[4:5]
	s_load_dwordx2 s[4:5], s[34:35], 0x8
	v_add_u32_e32 v4, 0x400, v2
	v_cmp_gt_i32_e32 vcc, s3, v4
	v_mov_b32_e32 v103, 0
	v_mov_b32_e32 v104, -1
	v_mov_b32_e32 v107, -1
	v_mov_b32_e32 v108, 0
	s_and_saveexec_b64 s[10:11], vcc
	s_cbranch_execz .LBB1_11
	v_ashrrev_i32_e32 v5, 31, v4
	v_lshlrev_b64 v[4:5], 2, v[4:5]
	v_lshl_add_u64 v[6:7], s[8:9], 0, v[4:5]
	v_lshl_add_u64 v[4:5], s[6:7], 0, v[4:5]
	global_load_dword v107, v[6:7], off nt
	global_load_dword v108, v[4:5], off nt
.LBB1_11:
	s_or_b64 exec, exec, s[10:11]
	v_add_u32_e32 v2, 0x600, v2
	v_cmp_gt_i32_e32 vcc, s3, v2
	s_and_saveexec_b64 s[10:11], vcc
	s_cbranch_execz .LBB1_13
	v_ashrrev_i32_e32 v3, 31, v2
	v_lshlrev_b64 v[2:3], 2, v[2:3]
	v_lshl_add_u64 v[4:5], s[8:9], 0, v[2:3]
	v_lshl_add_u64 v[2:3], s[6:7], 0, v[2:3]
	global_load_dword v104, v[4:5], off nt
	global_load_dword v103, v[2:3], off nt

_Z5k_csrPKjPKiPiS3_:
	s_load_dwordx4 s[16:19], s[0:1], 0x0
	s_ashr_i32 s3, s2, 31
	s_lshl_b64 s[4:5], s[2:3], 2
	v_mov_b32_e32 v6, -1
	v_mov_b32_e32 v8, -1
	s_waitcnt lgkmcnt(0)
	s_add_u32 s4, s18, s4
	s_addc_u32 s5, s19, s5
	s_load_dwordx2 s[14:15], s[4:5], 0x0
	s_waitcnt lgkmcnt(0)
	v_add_u32_e32 v2, s14, v0
	v_cmp_gt_i32_e32 vcc, s15, v2
	s_and_saveexec_b64 s[4:5], vcc
	s_cbranch_execz .LBB2_2
	v_ashrrev_i32_e32 v3, 31, v2
	v_lshl_add_u64 v[4:5], v[2:3], 2, s[16:17]
	global_load_dword v8, v[4:5], off nt
.LBB2_2:
	s_or_b64 exec, exec, s[4:5]
	v_add_u32_e32 v4, 0x400, v2
	v_cmp_gt_i32_e32 vcc, s15, v4
	s_and_saveexec_b64 s[4:5], vcc
	s_cbranch_execz .LBB2_4
	v_ashrrev_i32_e32 v5, 31, v4
	v_lshl_add_u64 v[4:5], v[4:5], 2, s[16:17]
	global_load_dword v6, v[4:5], off nt
.LBB2_4:
	s_or_b64 exec, exec, s[4:5]
	v_add_u32_e32 v4, 0x800, v2
	v_cmp_gt_i32_e32 vcc, s15, v4
	v_mov_b32_e32 v1, -1
	v_mov_b32_e32 v7, -1
	s_and_saveexec_b64 s[4:5], vcc
	s_cbranch_execz .LBB2_6
	v_ashrrev_i32_e32 v5, 31, v4
	v_lshl_add_u64 v[4:5], v[4:5], 2, s[16:17]
	global_load_dword v7, v[4:5], off nt
.LBB2_6:
	s_or_b64 exec, exec, s[4:5]
	v_add_u32_e32 v4, 0xc00, v2
	v_cmp_gt_i32_e32 vcc, s15, v4
	s_and_saveexec_b64 s[4:5], vcc
	s_cbranch_execz .LBB2_8
	v_ashrrev_i32_e32 v5, 31, v4
	v_lshl_add_u64 v[4:5], v[4:5], 2, s[16:17]
	global_load_dword v1, v[4:5], off nt

.LBB2_17:
	global_load_dword v12, v[4:5], off nt
	v_add_u32_e32 v11, 0x400, v11
	v_cmp_le_i32_e64 s[0:1], s15, v11
	s_or_b64 s[24:25], s[0:1], s[24:25]
	v_lshl_add_u64 v[4:5], v[4:5], 0, s[26:27]
	s_waitcnt vmcnt(0)
	v_lshlrev_b32_sdwa v12, v10, v12 dst_sel:DWORD dst_unused:UNUSED_PAD src0_sel:DWORD src1_sel:WORD_1
	ds_add_u32 v12, v9 offset:1024
	s_andn2_b64 exec, exec, s[24:25]
	s_cbranch_execnz .LBB2_17
